# LN1/router: top-4 by rank counting in every half-wave (one token per half-wave) instead of a serial 4-pass selection on 16 lanes of wave 0; one workgroup barrier fewer per token group
# baseline (speedup 1.0000x reference)
; #define LAS __attribute__((address_space(3)))
; template <bool SKIP_MIX>
; __device__ __forceinline__ void p8_ln_router(Frame& F0, const In& I) {
;     ...
;         f32x4 c0 = (f32x4){0.f, 0.f, 0.f, 0.f}, c1 = c0;
;         const LAS float* ap = hs + col * P8_PITCH + 256 * w + 4 * kq;
;         const float* bp = I.w_router + (size_t)(256 * w + 4 * kq) * NE + col;
; #pragma unroll 4
;         for (int kk = 0; kk < 16; ++kk) {
;             const f32x4 a = *(const LAS f32x4*)(ap + 16 * kk);
; #pragma unroll
;             for (int e = 0; e < 4; ++e) {
;                 const float b0 = bp[(size_t)(16 * kk + e) * NE], b1 = bp[(size_t)(16 * kk + e) * NE + 16];
;                 c0 = __builtin_amdgcn_mfma_f32_16x16x4f32(a[e], b0, c0, 0, 0, 0);
;                 c1 = __builtin_amdgcn_mfma_f32_16x16x4f32(a[e], b1, c1, 0, 0, 0);
;             }
;         }
.LBB0_1515:
	s_waitcnt vmcnt(19)
	s_mov_b64 s[0:1], 0x1000
	v_mov_b32_e32 v108, v88
	v_mov_b32_e32 v109, v89
	global_load_dword v117, v[108:109], off offset:0
	global_load_dword v118, v[108:109], off offset:64
	global_load_dword v119, v[108:109], off offset:128
	global_load_dword v120, v[108:109], off offset:192
	global_load_dword v121, v[108:109], off offset:256
	global_load_dword v122, v[108:109], off offset:320
	global_load_dword v123, v[108:109], off offset:384
	global_load_dword v124, v[108:109], off offset:448
	global_load_dword v125, v[108:109], off offset:2048
	global_load_dword v126, v[108:109], off offset:2112
	global_load_dword v127, v[108:109], off offset:2176
	global_load_dword v128, v[108:109], off offset:2240
	global_load_dword v129, v[108:109], off offset:2304
	global_load_dword v130, v[108:109], off offset:2368
	global_load_dword v131, v[108:109], off offset:2432
	global_load_dword v132, v[108:109], off offset:2496
	v_lshl_add_u64 v[108:109], v[108:109], 0, s[0:1]
	global_load_dword v133, v[108:109], off offset:0
	global_load_dword v134, v[108:109], off offset:64
	global_load_dword v135, v[108:109], off offset:128
	global_load_dword v136, v[108:109], off offset:192
	global_load_dword v137, v[108:109], off offset:256
	global_load_dword v138, v[108:109], off offset:320
	global_load_dword v139, v[108:109], off offset:384
	global_load_dword v140, v[108:109], off offset:448
	global_load_dword v141, v[108:109], off offset:2048
	global_load_dword v142, v[108:109], off offset:2112
	global_load_dword v143, v[108:109], off offset:2176
	global_load_dword v144, v[108:109], off offset:2240
	global_load_dword v145, v[108:109], off offset:2304
	global_load_dword v146, v[108:109], off offset:2368
	global_load_dword v147, v[108:109], off offset:2432
	global_load_dword v148, v[108:109], off offset:2496
	v_lshl_add_u64 v[108:109], v[108:109], 0, s[0:1]
	global_load_dword v149, v[108:109], off offset:0
	global_load_dword v150, v[108:109], off offset:64
	global_load_dword v151, v[108:109], off offset:128
	global_load_dword v160, v[108:109], off offset:192
	global_load_dword v161, v[108:109], off offset:256
	global_load_dword v162, v[108:109], off offset:320
	global_load_dword v163, v[108:109], off offset:384
	global_load_dword v164, v[108:109], off offset:448
	global_load_dword v165, v[108:109], off offset:2048
	global_load_dword v166, v[108:109], off offset:2112
	global_load_dword v167, v[108:109], off offset:2176
	global_load_dword v168, v[108:109], off offset:2240
	ds_read_b128 v[92:95], v90
	ds_read_b128 v[96:99], v90 offset:64
	ds_read_b128 v[100:103], v90 offset:128
	ds_read_b128 v[104:107], v90 offset:192
	s_waitcnt lgkmcnt(3)
	global_load_dword v169, v[108:109], off offset:2304
	s_waitcnt vmcnt(43)
	v_mfma_f32_16x16x4_f32 v[66:69], v92, v117, v[66:69]
	v_mfma_f32_16x16x4_f32 v[70:73], v92, v118, v[70:73]
	global_load_dword v170, v[108:109], off offset:2368
	s_waitcnt vmcnt(42)
	v_mfma_f32_16x16x4_f32 v[66:69], v93, v119, v[66:69]
	v_mfma_f32_16x16x4_f32 v[70:73], v93, v120, v[70:73]
	global_load_dword v171, v[108:109], off offset:2432
	s_waitcnt vmcnt(41)
	v_mfma_f32_16x16x4_f32 v[66:69], v94, v121, v[66:69]
	v_mfma_f32_16x16x4_f32 v[70:73], v94, v122, v[70:73]
	global_load_dword v172, v[108:109], off offset:2496
	s_waitcnt vmcnt(40)
	v_mfma_f32_16x16x4_f32 v[66:69], v95, v123, v[66:69]
	v_mfma_f32_16x16x4_f32 v[70:73], v95, v124, v[70:73]
	s_waitcnt lgkmcnt(2)
	v_lshl_add_u64 v[108:109], v[108:109], 0, s[0:1]
	global_load_dword v173, v[108:109], off offset:0
	s_waitcnt vmcnt(39)
	v_mfma_f32_16x16x4_f32 v[66:69], v96, v125, v[66:69]
	v_mfma_f32_16x16x4_f32 v[70:73], v96, v126, v[70:73]
	global_load_dword v174, v[108:109], off offset:64
	s_waitcnt vmcnt(38)
	v_mfma_f32_16x16x4_f32 v[66:69], v97, v127, v[66:69]
	v_mfma_f32_16x16x4_f32 v[70:73], v97, v128, v[70:73]
	global_load_dword v175, v[108:109], off offset:128
	s_waitcnt vmcnt(37)
	v_mfma_f32_16x16x4_f32 v[66:69], v98, v129, v[66:69]
	v_mfma_f32_16x16x4_f32 v[70:73], v98, v130, v[70:73]
	global_load_dword v176, v[108:109], off offset:192
	s_waitcnt vmcnt(36)
	v_mfma_f32_16x16x4_f32 v[66:69], v99, v131, v[66:69]
	v_mfma_f32_16x16x4_f32 v[70:73], v99, v132, v[70:73]
	s_waitcnt lgkmcnt(1)
	global_load_dword v177, v[108:109], off offset:256
	s_waitcnt vmcnt(35)
	v_mfma_f32_16x16x4_f32 v[66:69], v100, v133, v[66:69]
	v_mfma_f32_16x16x4_f32 v[70:73], v100, v134, v[70:73]
	global_load_dword v178, v[108:109], off offset:320
	s_waitcnt vmcnt(34)
	v_mfma_f32_16x16x4_f32 v[66:69], v101, v135, v[66:69]
	v_mfma_f32_16x16x4_f32 v[70:73], v101, v136, v[70:73]
	global_load_dword v179, v[108:109], off offset:384
	s_waitcnt vmcnt(33)
	v_mfma_f32_16x16x4_f32 v[66:69], v102, v137, v[66:69]
	v_mfma_f32_16x16x4_f32 v[70:73], v102, v138, v[70:73]
	global_load_dword v180, v[108:109], off offset:448
	s_waitcnt vmcnt(32)
	v_mfma_f32_16x16x4_f32 v[66:69], v103, v139, v[66:69]
	v_mfma_f32_16x16x4_f32 v[70:73], v103, v140, v[70:73]
	s_waitcnt lgkmcnt(0)
	global_load_dword v181, v[108:109], off offset:2048
	s_waitcnt vmcnt(31)
	v_mfma_f32_16x16x4_f32 v[66:69], v104, v141, v[66:69]
	v_mfma_f32_16x16x4_f32 v[70:73], v104, v142, v[70:73]
	global_load_dword v182, v[108:109], off offset:2112
	s_waitcnt vmcnt(30)
	v_mfma_f32_16x16x4_f32 v[66:69], v105, v143, v[66:69]
	v_mfma_f32_16x16x4_f32 v[70:73], v105, v144, v[70:73]
	global_load_dword v183, v[108:109], off offset:2176
	s_waitcnt vmcnt(29)
	v_mfma_f32_16x16x4_f32 v[66:69], v106, v145, v[66:69]
	v_mfma_f32_16x16x4_f32 v[70:73], v106, v146, v[70:73]
	global_load_dword v184, v[108:109], off offset:2240
	s_waitcnt vmcnt(28)
; #define LAS __attribute__((address_space(3)))
; template <bool SKIP_MIX>
; __device__ __forceinline__ void p8_ln_router(Frame& F0, const In& I) {
;     ...
;         for (int kk = 0; kk < 16; ++kk) {
;             const f32x4 a = *(const LAS f32x4*)(ap + 16 * kk);
; #pragma unroll
;             for (int e = 0; e < 4; ++e) {
;                 const float b0 = bp[(size_t)(16 * kk + e) * NE], b1 = bp[(size_t)(16 * kk + e) * NE + 16];
;                 c0 = __builtin_amdgcn_mfma_f32_16x16x4f32(a[e], b0, c0, 0, 0, 0);
;                 c1 = __builtin_amdgcn_mfma_f32_16x16x4f32(a[e], b1, c1, 0, 0, 0);
;             }
;         }
	v_mfma_f32_16x16x4_f32 v[66:69], v107, v147, v[66:69]
	v_mfma_f32_16x16x4_f32 v[70:73], v107, v148, v[70:73]
	ds_read_b128 v[92:95], v90 offset:256
	ds_read_b128 v[96:99], v90 offset:320
	ds_read_b128 v[100:103], v90 offset:384
	ds_read_b128 v[104:107], v90 offset:448
	s_waitcnt lgkmcnt(3)
	global_load_dword v185, v[108:109], off offset:2304
	s_waitcnt vmcnt(27)
	v_mfma_f32_16x16x4_f32 v[66:69], v92, v149, v[66:69]
	v_mfma_f32_16x16x4_f32 v[70:73], v92, v150, v[70:73]
	global_load_dword v186, v[108:109], off offset:2368
	s_waitcnt vmcnt(26)
	v_mfma_f32_16x16x4_f32 v[66:69], v93, v151, v[66:69]
	v_mfma_f32_16x16x4_f32 v[70:73], v93, v160, v[70:73]
	global_load_dword v187, v[108:109], off offset:2432
	s_waitcnt vmcnt(25)
	v_mfma_f32_16x16x4_f32 v[66:69], v94, v161, v[66:69]
	v_mfma_f32_16x16x4_f32 v[70:73], v94, v162, v[70:73]
	global_load_dword v188, v[108:109], off offset:2496
	s_waitcnt vmcnt(24)
	v_mfma_f32_16x16x4_f32 v[66:69], v95, v163, v[66:69]
	v_mfma_f32_16x16x4_f32 v[70:73], v95, v164, v[70:73]
	s_waitcnt lgkmcnt(2)
	v_lshl_add_u64 v[108:109], v[108:109], 0, s[0:1]
	global_load_dword v189, v[108:109], off offset:0
	s_waitcnt vmcnt(23)
	v_mfma_f32_16x16x4_f32 v[66:69], v96, v165, v[66:69]
	v_mfma_f32_16x16x4_f32 v[70:73], v96, v166, v[70:73]
	global_load_dword v190, v[108:109], off offset:64
	s_waitcnt vmcnt(22)
	v_mfma_f32_16x16x4_f32 v[66:69], v97, v167, v[66:69]
	v_mfma_f32_16x16x4_f32 v[70:73], v97, v168, v[70:73]
	global_load_dword v191, v[108:109], off offset:128
	s_waitcnt vmcnt(21)
	v_mfma_f32_16x16x4_f32 v[66:69], v98, v169, v[66:69]
	v_mfma_f32_16x16x4_f32 v[70:73], v98, v170, v[70:73]
	global_load_dword v192, v[108:109], off offset:192
	s_waitcnt vmcnt(20)
	v_mfma_f32_16x16x4_f32 v[66:69], v99, v171, v[66:69]
	v_mfma_f32_16x16x4_f32 v[70:73], v99, v172, v[70:73]
	s_waitcnt lgkmcnt(1)
	global_load_dword v193, v[108:109], off offset:256
	s_waitcnt vmcnt(19)
	v_mfma_f32_16x16x4_f32 v[66:69], v100, v173, v[66:69]
	v_mfma_f32_16x16x4_f32 v[70:73], v100, v174, v[70:73]
	global_load_dword v194, v[108:109], off offset:320
	s_waitcnt vmcnt(18)
	v_mfma_f32_16x16x4_f32 v[66:69], v101, v175, v[66:69]
	v_mfma_f32_16x16x4_f32 v[70:73], v101, v176, v[70:73]
	global_load_dword v195, v[108:109], off offset:384
	s_waitcnt vmcnt(17)
	v_mfma_f32_16x16x4_f32 v[66:69], v102, v177, v[66:69]
	v_mfma_f32_16x16x4_f32 v[70:73], v102, v178, v[70:73]
	global_load_dword v196, v[108:109], off offset:448
	s_waitcnt vmcnt(16)
	v_mfma_f32_16x16x4_f32 v[66:69], v103, v179, v[66:69]
	v_mfma_f32_16x16x4_f32 v[70:73], v103, v180, v[70:73]
	s_waitcnt lgkmcnt(0)
	global_load_dword v197, v[108:109], off offset:2048
	s_waitcnt vmcnt(15)
	v_mfma_f32_16x16x4_f32 v[66:69], v104, v181, v[66:69]
	v_mfma_f32_16x16x4_f32 v[70:73], v104, v182, v[70:73]
	global_load_dword v198, v[108:109], off offset:2112
	s_waitcnt vmcnt(14)
	v_mfma_f32_16x16x4_f32 v[66:69], v105, v183, v[66:69]
	v_mfma_f32_16x16x4_f32 v[70:73], v105, v184, v[70:73]
	global_load_dword v199, v[108:109], off offset:2176
	s_waitcnt vmcnt(13)
	v_mfma_f32_16x16x4_f32 v[66:69], v106, v185, v[66:69]
	v_mfma_f32_16x16x4_f32 v[70:73], v106, v186, v[70:73]
	s_waitcnt vmcnt(11)
	v_mfma_f32_16x16x4_f32 v[66:69], v107, v187, v[66:69]
	v_mfma_f32_16x16x4_f32 v[70:73], v107, v188, v[70:73]
	ds_read_b128 v[92:95], v90 offset:512
	ds_read_b128 v[96:99], v90 offset:576
	ds_read_b128 v[100:103], v90 offset:640
	ds_read_b128 v[104:107], v90 offset:704
	s_waitcnt lgkmcnt(3)
	s_waitcnt vmcnt(9)
	v_mfma_f32_16x16x4_f32 v[66:69], v92, v189, v[66:69]
	v_mfma_f32_16x16x4_f32 v[70:73], v92, v190, v[70:73]
	s_waitcnt vmcnt(7)
	v_mfma_f32_16x16x4_f32 v[66:69], v93, v191, v[66:69]
	v_mfma_f32_16x16x4_f32 v[70:73], v93, v192, v[70:73]
	s_waitcnt vmcnt(5)
	v_mfma_f32_16x16x4_f32 v[66:69], v94, v193, v[66:69]
	v_mfma_f32_16x16x4_f32 v[70:73], v94, v194, v[70:73]
	s_waitcnt vmcnt(3)
	v_mfma_f32_16x16x4_f32 v[66:69], v95, v195, v[66:69]
	v_mfma_f32_16x16x4_f32 v[70:73], v95, v196, v[70:73]
	s_waitcnt lgkmcnt(2)
	s_waitcnt vmcnt(1)
	v_mfma_f32_16x16x4_f32 v[66:69], v96, v197, v[66:69]
	v_mfma_f32_16x16x4_f32 v[70:73], v96, v198, v[70:73]
	s_waitcnt vmcnt(0)
	v_mfma_f32_16x16x4_f32 v[66:69], v97, v199, v[66:69]
	v_mfma_f32_16x16x4_f32 v[70:73], v97, v200, v[70:73]
	v_mfma_f32_16x16x4_f32 v[66:69], v98, v201, v[66:69]
	v_mfma_f32_16x16x4_f32 v[70:73], v98, v202, v[70:73]
	v_mfma_f32_16x16x4_f32 v[66:69], v99, v203, v[66:69]
	v_mfma_f32_16x16x4_f32 v[70:73], v99, v204, v[70:73]
	s_waitcnt lgkmcnt(1)
	v_mfma_f32_16x16x4_f32 v[66:69], v100, v205, v[66:69]
	v_mfma_f32_16x16x4_f32 v[70:73], v100, v206, v[70:73]
	v_mfma_f32_16x16x4_f32 v[66:69], v101, v207, v[66:69]
	v_mfma_f32_16x16x4_f32 v[70:73], v101, v208, v[70:73]
	v_mfma_f32_16x16x4_f32 v[66:69], v102, v209, v[66:69]
	v_mfma_f32_16x16x4_f32 v[70:73], v102, v210, v[70:73]
	v_mfma_f32_16x16x4_f32 v[66:69], v103, v211, v[66:69]
	v_mfma_f32_16x16x4_f32 v[70:73], v103, v212, v[70:73]
	s_waitcnt lgkmcnt(0)
	v_mfma_f32_16x16x4_f32 v[66:69], v104, v213, v[66:69]
	v_mfma_f32_16x16x4_f32 v[70:73], v104, v214, v[70:73]
	v_mfma_f32_16x16x4_f32 v[66:69], v105, v215, v[66:69]
	v_mfma_f32_16x16x4_f32 v[70:73], v105, v216, v[70:73]
	v_mfma_f32_16x16x4_f32 v[66:69], v106, v217, v[66:69]
	v_mfma_f32_16x16x4_f32 v[70:73], v106, v218, v[70:73]
	v_mfma_f32_16x16x4_f32 v[66:69], v107, v219, v[66:69]
	v_mfma_f32_16x16x4_f32 v[70:73], v107, v220, v[70:73]
	ds_read_b128 v[92:95], v90 offset:768
	ds_read_b128 v[96:99], v90 offset:832
	ds_read_b128 v[100:103], v90 offset:896
	ds_read_b128 v[104:107], v90 offset:960
	s_waitcnt lgkmcnt(3)
; template <bool SKIP_MIX>
; __device__ __forceinline__ void p8_ln_router(Frame& F0, const In& I) {
;     ...
; #pragma unroll
;         for (int i = 0; i < 4; ++i) { part[(w * 16 + 4 * kq + i) * 32 + col] = c0[i]; part[(w * 16 + 4 * kq + i) * 32 + 16 + col] = c1[i]; }
;         __syncthreads();
;         { const int tl = F.tid >> 5, e = F.tid & 31; float s = I.b_router[e];
; #pragma unroll
;             for (int ww = 0; ww < 8; ++ww) s += part[(ww * 16 + tl) * 32 + e];
;             lg[tl * 32 + e] = s; }
;         __syncthreads();
;         if (F.tid < 16) {
;             const int tl = F.tid; float lv[32];
; #pragma unroll
;             for (int e = 0; e < 32; ++e) lv[e] = lg[tl * 32 + e];
;             int ti[4]; float tv[4];
; #pragma unroll
;             for (int k = 0; k < 4; ++k) { float best = -3.4e38f; int bi = 0;
; #pragma unroll
;                 for (int e = 0; e < 32; ++e) { const bool tk = lv[e] > best; best = tk ? lv[e] : best; bi = tk ? e : bi; }
;                 ti[k] = bi; tv[k] = best;
; #pragma unroll
;                 for (int e = 0; e < 32; ++e) lv[e] = (e == bi) ? -3.4e38f : lv[e]; }
	v_mfma_f32_16x16x4_f32 v[66:69], v92, v221, v[66:69]
	v_mfma_f32_16x16x4_f32 v[70:73], v92, v222, v[70:73]
	v_mfma_f32_16x16x4_f32 v[66:69], v93, v223, v[66:69]
	v_mfma_f32_16x16x4_f32 v[70:73], v93, v224, v[70:73]
	v_mfma_f32_16x16x4_f32 v[66:69], v94, v225, v[66:69]
	v_mfma_f32_16x16x4_f32 v[70:73], v94, v226, v[70:73]
	v_mfma_f32_16x16x4_f32 v[66:69], v95, v227, v[66:69]
	v_mfma_f32_16x16x4_f32 v[70:73], v95, v228, v[70:73]
	s_waitcnt lgkmcnt(2)
	v_mfma_f32_16x16x4_f32 v[66:69], v96, v229, v[66:69]
	v_mfma_f32_16x16x4_f32 v[70:73], v96, v230, v[70:73]
	v_mfma_f32_16x16x4_f32 v[66:69], v97, v231, v[66:69]
	v_mfma_f32_16x16x4_f32 v[70:73], v97, v232, v[70:73]
	v_mfma_f32_16x16x4_f32 v[66:69], v98, v233, v[66:69]
	v_mfma_f32_16x16x4_f32 v[70:73], v98, v234, v[70:73]
	v_mfma_f32_16x16x4_f32 v[66:69], v99, v235, v[66:69]
	v_mfma_f32_16x16x4_f32 v[70:73], v99, v236, v[70:73]
	s_waitcnt lgkmcnt(1)
	v_mfma_f32_16x16x4_f32 v[66:69], v100, v237, v[66:69]
	v_mfma_f32_16x16x4_f32 v[70:73], v100, v238, v[70:73]
	v_mfma_f32_16x16x4_f32 v[66:69], v101, v239, v[66:69]
	v_mfma_f32_16x16x4_f32 v[70:73], v101, v240, v[70:73]
	v_mfma_f32_16x16x4_f32 v[66:69], v102, v241, v[66:69]
	v_mfma_f32_16x16x4_f32 v[70:73], v102, v242, v[70:73]
	v_mfma_f32_16x16x4_f32 v[66:69], v103, v243, v[66:69]
	v_mfma_f32_16x16x4_f32 v[70:73], v103, v244, v[70:73]
	s_waitcnt lgkmcnt(0)
	v_mfma_f32_16x16x4_f32 v[66:69], v104, v245, v[66:69]
	v_mfma_f32_16x16x4_f32 v[70:73], v104, v246, v[70:73]
	v_mfma_f32_16x16x4_f32 v[66:69], v105, v247, v[66:69]
	v_mfma_f32_16x16x4_f32 v[70:73], v105, v248, v[70:73]
	v_mfma_f32_16x16x4_f32 v[66:69], v106, v249, v[66:69]
	v_mfma_f32_16x16x4_f32 v[70:73], v106, v250, v[70:73]
	v_mfma_f32_16x16x4_f32 v[66:69], v107, v251, v[66:69]
	v_mfma_f32_16x16x4_f32 v[70:73], v107, v252, v[70:73]
	s_nop 8
	ds_write2_b32 v156, v66, v70 offset1:16
	ds_write2_b32 v156, v67, v71 offset0:32 offset1:48
	ds_write2_b32 v156, v68, v72 offset0:64 offset1:80
	ds_write2_b32 v156, v69, v73 offset0:96 offset1:112
	s_waitcnt lgkmcnt(0)
	s_barrier
	ds_read2st64_b32 v[66:67], v153 offset1:8
	ds_read2st64_b32 v[68:69], v153 offset0:16 offset1:24
	ds_read2st64_b32 v[70:71], v153 offset0:32 offset1:40
	ds_read2st64_b32 v[72:73], v153 offset0:48 offset1:56
	s_waitcnt lgkmcnt(3)
	v_add_f32_e32 v66, v253, v66
	v_add_f32_e32 v66, v66, v67
	s_waitcnt lgkmcnt(2)
	v_add_f32_e32 v66, v66, v68
	v_add_f32_e32 v66, v66, v69
	s_waitcnt lgkmcnt(1)
	v_add_f32_e32 v66, v66, v70
	v_add_f32_e32 v66, v66, v71
	s_waitcnt lgkmcnt(0)
	v_add_f32_e32 v66, v66, v72
	v_add_f32_e32 v66, v66, v73
	ds_write_b32 v154, v66
	s_waitcnt lgkmcnt(0)
	s_mov_b64 s[0:1], exec
	v_and_b32_e32 v194, 0xffffff80, v154
	ds_read_b128 v[160:163], v194
	ds_read_b128 v[164:167], v194 offset:16
	ds_read_b128 v[168:171], v194 offset:32
	ds_read_b128 v[172:175], v194 offset:48
	ds_read_b128 v[176:179], v194 offset:64
	ds_read_b128 v[180:183], v194 offset:80
	ds_read_b128 v[184:187], v194 offset:96
	ds_read_b128 v[188:191], v194 offset:112
	v_and_b32_e32 v192, 31, v74
	v_mov_b32_e32 v193, 0
	s_waitcnt lgkmcnt(0)
	v_cmp_gt_f32_e64 s[24:25], v160, v66
	v_cmp_ge_f32_e64 s[26:27], v160, v66
	s_and_b32 s26, s26, 0xfffffffe
	s_and_b32 s27, s27, 0xfffffffe
	s_or_b64 vcc, s[24:25], s[26:27]
	v_cmp_gt_f32_e64 s[32:33], v161, v66
	v_cmp_ge_f32_e64 s[34:35], v161, v66
	v_addc_co_u32_e32 v193, vcc, 0, v193, vcc
	s_and_b32 s34, s34, 0xfffffffc
	s_and_b32 s35, s35, 0xfffffffc
	s_or_b64 vcc, s[32:33], s[34:35]
	v_cmp_gt_f32_e64 s[24:25], v162, v66
	v_cmp_ge_f32_e64 s[26:27], v162, v66
	v_addc_co_u32_e32 v193, vcc, 0, v193, vcc
	s_and_b32 s26, s26, 0xfffffff8
	s_and_b32 s27, s27, 0xfffffff8
	s_or_b64 vcc, s[24:25], s[26:27]
	v_cmp_gt_f32_e64 s[32:33], v163, v66
	v_cmp_ge_f32_e64 s[34:35], v163, v66
	v_addc_co_u32_e32 v193, vcc, 0, v193, vcc
	s_and_b32 s34, s34, 0xfffffff0
	s_and_b32 s35, s35, 0xfffffff0
	s_or_b64 vcc, s[32:33], s[34:35]
	v_cmp_gt_f32_e64 s[24:25], v164, v66
	v_cmp_ge_f32_e64 s[26:27], v164, v66
	v_addc_co_u32_e32 v193, vcc, 0, v193, vcc
	s_and_b32 s26, s26, 0xffffffe0
	s_and_b32 s27, s27, 0xffffffe0
	s_or_b64 vcc, s[24:25], s[26:27]
	v_cmp_gt_f32_e64 s[32:33], v165, v66
	v_cmp_ge_f32_e64 s[34:35], v165, v66
	v_addc_co_u32_e32 v193, vcc, 0, v193, vcc
	s_and_b32 s34, s34, 0xffffffc0
	s_and_b32 s35, s35, 0xffffffc0
	s_or_b64 vcc, s[32:33], s[34:35]
	v_cmp_gt_f32_e64 s[24:25], v166, v66
	v_cmp_ge_f32_e64 s[26:27], v166, v66
	v_addc_co_u32_e32 v193, vcc, 0, v193, vcc
	s_and_b32 s26, s26, 0xffffff80
	s_and_b32 s27, s27, 0xffffff80
	s_or_b64 vcc, s[24:25], s[26:27]
	v_cmp_gt_f32_e64 s[32:33], v167, v66
	v_cmp_ge_f32_e64 s[34:35], v167, v66
	v_addc_co_u32_e32 v193, vcc, 0, v193, vcc
	s_and_b32 s34, s34, 0xffffff00
	s_and_b32 s35, s35, 0xffffff00
	s_or_b64 vcc, s[32:33], s[34:35]
	v_cmp_gt_f32_e64 s[24:25], v168, v66
	v_cmp_ge_f32_e64 s[26:27], v168, v66
	v_addc_co_u32_e32 v193, vcc, 0, v193, vcc
	s_and_b32 s26, s26, 0xfffffe00
	s_and_b32 s27, s27, 0xfffffe00
	s_or_b64 vcc, s[24:25], s[26:27]
	v_cmp_gt_f32_e64 s[32:33], v169, v66
	v_cmp_ge_f32_e64 s[34:35], v169, v66
	v_addc_co_u32_e32 v193, vcc, 0, v193, vcc
	s_and_b32 s34, s34, 0xfffffc00
	s_and_b32 s35, s35, 0xfffffc00
	s_or_b64 vcc, s[32:33], s[34:35]
	v_cmp_gt_f32_e64 s[24:25], v170, v66
	v_cmp_ge_f32_e64 s[26:27], v170, v66
	v_addc_co_u32_e32 v193, vcc, 0, v193, vcc
	s_and_b32 s26, s26, 0xfffff800
	s_and_b32 s27, s27, 0xfffff800
	s_or_b64 vcc, s[24:25], s[26:27]
	v_cmp_gt_f32_e64 s[32:33], v171, v66
	v_cmp_ge_f32_e64 s[34:35], v171, v66
	v_addc_co_u32_e32 v193, vcc, 0, v193, vcc
	s_and_b32 s34, s34, 0xfffff000
	s_and_b32 s35, s35, 0xfffff000
	s_or_b64 vcc, s[32:33], s[34:35]
; #define GAS __attribute__((address_space(1)))
; template <bool SKIP_MIX>
; __device__ __forceinline__ void p8_ln_router(Frame& F0, const In& I) {
;     ...
;             for (int k = 0; k < 4; ++k) { float best = -3.4e38f; int bi = 0;
; #pragma unroll
;                 for (int e = 0; e < 32; ++e) { const bool tk = lv[e] > best; best = tk ? lv[e] : best; bi = tk ? e : bi; }
;                 ti[k] = bi; tv[k] = best;
; #pragma unroll
;                 for (int e = 0; e < 32; ++e) lv[e] = (e == bi) ? -3.4e38f : lv[e]; }
;             float ex[4], sum = 0.f;
; #pragma unroll
;             for (int k = 0; k < 4; ++k) { ex[k] = __expf(tv[k] - tv[0]); sum += ex[k]; }
;             const float inv = 1.f / sum;
;             *(GAS v4u*)((int*)(F.ws + WS_TOPI) + (size_t)(tok0 + tl) * 4) = (v4u){(unsigned)ti[0], (unsigned)ti[1], (unsigned)ti[2], (unsigned)ti[3]};
;             *(GAS f32x4*)((float*)(F.ws + WS_GATE) + (size_t)(tok0 + tl) * 4) = (f32x4){ex[0] * inv, ex[1] * inv, ex[2] * inv, ex[3] * inv};
; #pragma unroll
;             for (int k = 0; k < 4; ++k) __hip_atomic_fetch_add(&hist[ti[k]], 1, __ATOMIC_RELAXED, __HIP_MEMORY_SCOPE_WORKGROUP);
;         }
;         __syncthreads();
;     ...
;     if (F.tid < 32) { const int c = hist[F.tid]; if (c) __hip_atomic_fetch_add(F.ctl + CW_CNT + F.tid, (unsigned)c, RLX_AGENT); }
	v_cmp_gt_f32_e64 s[24:25], v172, v66
	v_cmp_ge_f32_e64 s[26:27], v172, v66
	v_addc_co_u32_e32 v193, vcc, 0, v193, vcc
	s_and_b32 s26, s26, 0xffffe000
	s_and_b32 s27, s27, 0xffffe000
	s_or_b64 vcc, s[24:25], s[26:27]
	v_cmp_gt_f32_e64 s[32:33], v173, v66
	v_cmp_ge_f32_e64 s[34:35], v173, v66
	v_addc_co_u32_e32 v193, vcc, 0, v193, vcc
	s_and_b32 s34, s34, 0xffffc000
	s_and_b32 s35, s35, 0xffffc000
	s_or_b64 vcc, s[32:33], s[34:35]
	v_cmp_gt_f32_e64 s[24:25], v174, v66
	v_cmp_ge_f32_e64 s[26:27], v174, v66
	v_addc_co_u32_e32 v193, vcc, 0, v193, vcc
	s_and_b32 s26, s26, 0xffff8000
	s_and_b32 s27, s27, 0xffff8000
	s_or_b64 vcc, s[24:25], s[26:27]
	v_cmp_gt_f32_e64 s[32:33], v175, v66
	v_cmp_ge_f32_e64 s[34:35], v175, v66
	v_addc_co_u32_e32 v193, vcc, 0, v193, vcc
	s_and_b32 s34, s34, 0xffff0000
	s_and_b32 s35, s35, 0xffff0000
	s_or_b64 vcc, s[32:33], s[34:35]
	v_cmp_gt_f32_e64 s[24:25], v176, v66
	v_cmp_ge_f32_e64 s[26:27], v176, v66
	v_addc_co_u32_e32 v193, vcc, 0, v193, vcc
	s_and_b32 s26, s26, 0xfffe0000
	s_and_b32 s27, s27, 0xfffe0000
	s_or_b64 vcc, s[24:25], s[26:27]
	v_cmp_gt_f32_e64 s[32:33], v177, v66
	v_cmp_ge_f32_e64 s[34:35], v177, v66
	v_addc_co_u32_e32 v193, vcc, 0, v193, vcc
	s_and_b32 s34, s34, 0xfffc0000
	s_and_b32 s35, s35, 0xfffc0000
	s_or_b64 vcc, s[32:33], s[34:35]
	v_cmp_gt_f32_e64 s[24:25], v178, v66
	v_cmp_ge_f32_e64 s[26:27], v178, v66
	v_addc_co_u32_e32 v193, vcc, 0, v193, vcc
	s_and_b32 s26, s26, 0xfff80000
	s_and_b32 s27, s27, 0xfff80000
	s_or_b64 vcc, s[24:25], s[26:27]
	v_cmp_gt_f32_e64 s[32:33], v179, v66
	v_cmp_ge_f32_e64 s[34:35], v179, v66
	v_addc_co_u32_e32 v193, vcc, 0, v193, vcc
	s_and_b32 s34, s34, 0xfff00000
	s_and_b32 s35, s35, 0xfff00000
	s_or_b64 vcc, s[32:33], s[34:35]
	v_cmp_gt_f32_e64 s[24:25], v180, v66
	v_cmp_ge_f32_e64 s[26:27], v180, v66
	v_addc_co_u32_e32 v193, vcc, 0, v193, vcc
	s_and_b32 s26, s26, 0xffe00000
	s_and_b32 s27, s27, 0xffe00000
	s_or_b64 vcc, s[24:25], s[26:27]
	v_cmp_gt_f32_e64 s[32:33], v181, v66
	v_cmp_ge_f32_e64 s[34:35], v181, v66
	v_addc_co_u32_e32 v193, vcc, 0, v193, vcc
	s_and_b32 s34, s34, 0xffc00000
	s_and_b32 s35, s35, 0xffc00000
	s_or_b64 vcc, s[32:33], s[34:35]
	v_cmp_gt_f32_e64 s[24:25], v182, v66
	v_cmp_ge_f32_e64 s[26:27], v182, v66
	v_addc_co_u32_e32 v193, vcc, 0, v193, vcc
	s_and_b32 s26, s26, 0xff800000
	s_and_b32 s27, s27, 0xff800000
	s_or_b64 vcc, s[24:25], s[26:27]
	v_cmp_gt_f32_e64 s[32:33], v183, v66
	v_cmp_ge_f32_e64 s[34:35], v183, v66
	v_addc_co_u32_e32 v193, vcc, 0, v193, vcc
	s_and_b32 s34, s34, 0xff000000
	s_and_b32 s35, s35, 0xff000000
	s_or_b64 vcc, s[32:33], s[34:35]
	v_cmp_gt_f32_e64 s[24:25], v184, v66
	v_cmp_ge_f32_e64 s[26:27], v184, v66
	v_addc_co_u32_e32 v193, vcc, 0, v193, vcc
	s_and_b32 s26, s26, 0xfe000000
	s_and_b32 s27, s27, 0xfe000000
	s_or_b64 vcc, s[24:25], s[26:27]
	v_cmp_gt_f32_e64 s[32:33], v185, v66
	v_cmp_ge_f32_e64 s[34:35], v185, v66
	v_addc_co_u32_e32 v193, vcc, 0, v193, vcc
	s_and_b32 s34, s34, 0xfc000000
	s_and_b32 s35, s35, 0xfc000000
	s_or_b64 vcc, s[32:33], s[34:35]
	v_cmp_gt_f32_e64 s[24:25], v186, v66
	v_cmp_ge_f32_e64 s[26:27], v186, v66
	v_addc_co_u32_e32 v193, vcc, 0, v193, vcc
	s_and_b32 s26, s26, 0xf8000000
	s_and_b32 s27, s27, 0xf8000000
	s_or_b64 vcc, s[24:25], s[26:27]
	v_cmp_gt_f32_e64 s[32:33], v187, v66
	v_cmp_ge_f32_e64 s[34:35], v187, v66
	v_addc_co_u32_e32 v193, vcc, 0, v193, vcc
	s_and_b32 s34, s34, 0xf0000000
	s_and_b32 s35, s35, 0xf0000000
	s_or_b64 vcc, s[32:33], s[34:35]
	v_cmp_gt_f32_e64 s[24:25], v188, v66
	v_cmp_ge_f32_e64 s[26:27], v188, v66
	v_addc_co_u32_e32 v193, vcc, 0, v193, vcc
	s_and_b32 s26, s26, 0xe0000000
	s_and_b32 s27, s27, 0xe0000000
	s_or_b64 vcc, s[24:25], s[26:27]
	v_cmp_gt_f32_e64 s[32:33], v189, v66
	v_cmp_ge_f32_e64 s[34:35], v189, v66
	v_addc_co_u32_e32 v193, vcc, 0, v193, vcc
	s_and_b32 s34, s34, 0xc0000000
	s_and_b32 s35, s35, 0xc0000000
	s_or_b64 vcc, s[32:33], s[34:35]
	v_cmp_gt_f32_e64 s[24:25], v190, v66
	v_cmp_ge_f32_e64 s[26:27], v190, v66
	v_addc_co_u32_e32 v193, vcc, 0, v193, vcc
	s_and_b32 s26, s26, 0x80000000
	s_and_b32 s27, s27, 0x80000000
	s_or_b64 vcc, s[24:25], s[26:27]
	v_cmp_gt_f32_e64 s[32:33], v191, v66
	v_cmp_ge_f32_e64 s[34:35], v191, v66
	v_addc_co_u32_e32 v193, vcc, 0, v193, vcc
	s_and_b32 s34, s34, 0x0
	s_and_b32 s35, s35, 0x0
	s_or_b64 vcc, s[32:33], s[34:35]
	s_nop 1
	v_addc_co_u32_e32 v193, vcc, 0, v193, vcc
	v_cmp_gt_u32_e32 vcc, 4, v193
	s_and_saveexec_b64 s[28:29], vcc
	v_lshrrev_b32_e32 v195, 1, v74
	v_and_b32_e32 v195, 0xf0, v195
	v_lshl_add_u32 v195, v193, 2, v195
	v_add_u32_e32 v195, 0x24a00, v195
	ds_write_b32 v195, v192
	ds_write_b32 v195, v66 offset:256
	s_mov_b64 exec, s[0:1]
	s_waitcnt lgkmcnt(0)
	v_cmp_eq_u32_e32 vcc, 0, v192
	s_and_saveexec_b64 s[28:29], vcc
	v_lshrrev_b32_e32 v195, 1, v74
	v_and_b32_e32 v195, 0xf0, v195
	v_add_u32_e32 v195, 0x24a00, v195
	ds_read_b128 v[66:69], v195
	ds_read_b128 v[90:93], v195 offset:256
	v_lshrrev_b32_e32 v196, 5, v74
	s_waitcnt lgkmcnt(0)
	v_sub_f32_e32 v70, v90, v90
	v_sub_f32_e32 v71, v91, v90
	v_sub_f32_e32 v72, v92, v90
	v_sub_f32_e32 v73, v93, v90
	v_mul_f32_e32 v70, 0x3fb8aa3b, v70
	v_mul_f32_e32 v71, 0x3fb8aa3b, v71
	v_mul_f32_e32 v72, 0x3fb8aa3b, v72
	v_mul_f32_e32 v73, 0x3fb8aa3b, v73
	v_exp_f32_e32 v70, v70
	v_exp_f32_e32 v71, v71
	v_exp_f32_e32 v72, v72
	v_exp_f32_e32 v73, v73
	s_nop 1
	v_add_f32_e32 v90, 0, v70
	v_add_f32_e32 v90, v90, v71
	v_add_f32_e32 v90, v90, v72
	v_add_f32_e32 v90, v90, v73
	v_div_scale_f32 v91, s[14:15], v90, v90, 1.0
	v_rcp_f32_e32 v92, v91
	s_nop 0
	v_fma_f32 v93, -v91, v92, 1.0
	v_fmac_f32_e32 v92, v93, v92
	v_div_scale_f32 v93, vcc, 1.0, v90, 1.0
	v_mul_f32_e32 v94, v93, v92
	v_fma_f32 v95, -v91, v94, v93
	v_fmac_f32_e32 v94, v95, v92
	v_fma_f32 v91, -v91, v94, v93
	v_div_fmas_f32 v91, v91, v92, v94
	v_add_u32_e32 v92, s23, v196
	v_ashrrev_i32_e32 v93, 31, v92
	v_div_fixup_f32 v90, v91, v90, 1.0
	v_lshlrev_b64 v[92:93], 4, v[92:93]
	v_lshl_add_u64 v[94:95], s[6:7], 0, v[92:93]
	v_pk_mul_f32 v[72:73], v[72:73], v[90:91] op_sel_hi:[1,0]
	v_pk_mul_f32 v[70:71], v[70:71], v[90:91] op_sel_hi:[1,0]
	v_lshl_add_u64 v[90:91], s[10:11], 0, v[92:93]
	global_store_dwordx4 v[94:95], v[66:69], off
	global_store_dwordx4 v[90:91], v[70:73], off
	s_nop 0
	v_lshl_add_u32 v197, v66, 2, s21
	ds_add_u32 v197, v158
	v_lshl_add_u32 v197, v67, 2, s21
	ds_add_u32 v197, v158
	v_lshl_add_u32 v197, v68, 2, s21
	ds_add_u32 v197, v158
	v_lshl_add_u32 v197, v69, 2, s21
	ds_add_u32 v197, v158
	s_mov_b64 exec, s[0:1]
	s_branch .LBB0_1513
.LBB0_1518:
	s_barrier
	s_and_saveexec_b64 s[0:1], s[2:3]
	s_cbranch_execz .LBB0_1521
	v_add_u32_e32 v1, 0x24900, v1
	ds_read_b32 v1, v1
	s_waitcnt lgkmcnt(0)
	v_cmp_ne_u32_e32 vcc, 0, v1
	s_and_b64 exec, exec, vcc
	s_cbranch_execz .LBB0_1521
	v_ashrrev_i32_e32 v75, 31, v74
	s_waitcnt vmcnt(15)
	v_lshl_add_u64 v[2:3], v[74:75], 2, s[96:97]
	global_atomic_add v[2:3], v1, off offset:2048
